# barrier release: last leader bumps all per-XCD generation words directly
# baseline (speedup 1.0000x reference)
; __device__ __forceinline__ unsigned xb_ld(unsigned* p)              { return __hip_atomic_load(p, __ATOMIC_RELAXED, __HIP_MEMORY_SCOPE_AGENT); }
; __device__ __forceinline__ unsigned xb_add(unsigned* p, unsigned v) { return __hip_atomic_fetch_add(p, v, __ATOMIC_RELAXED, __HIP_MEMORY_SCOPE_AGENT); }
; #define XB_SPIN(cond, bar) do { unsigned _sp = 0; while (cond) { __builtin_amdgcn_s_sleep(1); \
;     if ((++_sp & 255u) == 0u) { if (xb_ld(&(bar)[XB_TMO])) break; if (_sp > XB_SPIN_CAP) { atomicAdd(&(bar)[XB_TMO], 1u); break; } } } } while (0)
; __device__ __forceinline__ void xcd_barrier(const XcdBarrier& b) {
;     ...
;         if (old + 1u == (gen + 1u) * nloc) {
;             __builtin_amdgcn_fence(__ATOMIC_RELEASE, "agent");
;             asm volatile("s_waitcnt vmcnt(0)" ::: "memory");
;             const unsigned og = xb_add(&bar[XB_TOP], 1u);
;             const unsigned tg = og / nx;
;             if (og + 1u == (tg + 1u) * nx) xb_add(&bar[XB_TOPGEN], 1u);
;             else XB_SPIN(xb_ld(&bar[XB_TOPGEN]) == tg, bar);
.LBB0_237:
	s_or_b64 exec, exec, s[6:7]
	s_waitcnt vmcnt(0)
	v_readfirstlane_b32 s4, v3
	v_sub_u32_e32 v4, 0, v2
	s_mov_b64 s[6:7], -1
	v_add_u32_e32 v3, s4, v1
	v_cvt_f32_u32_e32 v1, v2
	v_readlane_b32 s4, v251, 36
	v_readlane_b32 s5, v251, 37
	v_rcp_iflag_f32_e32 v1, v1
	s_nop 0
	v_mul_f32_e32 v1, 0x4f7ffffe, v1
	v_cvt_u32_f32_e32 v1, v1
	v_mul_lo_u32 v4, v4, v1
	v_mul_hi_u32 v4, v1, v4
	v_add_u32_e32 v1, v1, v4
	v_mul_hi_u32 v1, v3, v1
	v_mul_lo_u32 v4, v1, v2
	v_sub_u32_e32 v4, v3, v4
	v_cmp_ge_u32_e32 vcc, v4, v2
	v_add_u32_e32 v5, 1, v1
	v_add_u32_e32 v3, 1, v3
	v_cndmask_b32_e32 v1, v1, v5, vcc
	v_sub_u32_e32 v5, v4, v2
	v_cndmask_b32_e32 v4, v4, v5, vcc
	v_cmp_ge_u32_e32 vcc, v4, v2
	v_add_u32_e32 v4, 1, v1
	s_nop 0
	v_cndmask_b32_e32 v1, v1, v4, vcc
	v_mul_lo_u32 v4, v2, v1
	v_add_u32_e32 v2, v4, v2
	v_cmp_ne_u32_e32 vcc, v3, v2
	v_mov_b64_e32 v[2:3], s[4:5]
	s_and_saveexec_b64 s[4:5], vcc
	s_cbranch_execz .LBB0_249
	v_readlane_b32 s6, v251, 32
	v_readlane_b32 s7, v251, 33
	s_mov_b64 s[8:9], 0
	s_nop 3
	global_load_dword v2, v187, s[6:7] sc1
	s_waitcnt vmcnt(0)
	v_cmp_eq_u32_e32 vcc, v2, v1
	s_and_saveexec_b64 s[6:7], vcc
	s_cbranch_execz .LBB0_248
	s_mov_b32 s21, 1
	s_branch .LBB0_241

; __device__ __forceinline__ unsigned xb_ld(unsigned* p)              { return __hip_atomic_load(p, __ATOMIC_RELAXED, __HIP_MEMORY_SCOPE_AGENT); }
; __device__ __forceinline__ unsigned xb_add(unsigned* p, unsigned v) { return __hip_atomic_fetch_add(p, v, __ATOMIC_RELAXED, __HIP_MEMORY_SCOPE_AGENT); }
; #define XB_SPIN(cond, bar) do { unsigned _sp = 0; while (cond) { __builtin_amdgcn_s_sleep(1); \
;     if ((++_sp & 255u) == 0u) { if (xb_ld(&(bar)[XB_TMO])) break; if (_sp > XB_SPIN_CAP) { atomicAdd(&(bar)[XB_TMO], 1u); break; } } } } while (0)
; __device__ __forceinline__ void xcd_barrier(const XcdBarrier& b) {
;     ...
;             const unsigned og = xb_add(&bar[XB_TOP], 1u);
;             const unsigned tg = og / nx;
;             if (og + 1u == (tg + 1u) * nx) xb_add(&bar[XB_TOPGEN], 1u);
;             else XB_SPIN(xb_ld(&bar[XB_TOPGEN]) == tg, bar);
;             __builtin_amdgcn_fence(__ATOMIC_ACQUIRE, "agent");
;             xb_add(&bar[XB_XGEN(b.x)], 1u);
;             asm volatile("s_waitcnt vmcnt(0)" ::: "memory");
.LBB0_249:
	s_or_b64 exec, exec, s[4:5]
	s_and_saveexec_b64 s[4:5], s[6:7]
	s_cbranch_execz .LBB0_251
	global_atomic_add v[2:3], v224, off
	v_readlane_b32 s6, v250, 28
	v_readlane_b32 s7, v250, 29
	s_nop 0
	s_add_u32 s6, s6, 0x2200
	s_addc_u32 s7, s7, 0
	s_nop 0
	global_atomic_add v187, v224, s[6:7]
	global_atomic_add v187, v224, s[6:7] offset:256
	global_atomic_add v187, v224, s[6:7] offset:512
	global_atomic_add v187, v224, s[6:7] offset:768
	global_atomic_add v187, v224, s[6:7] offset:1024
	global_atomic_add v187, v224, s[6:7] offset:1280
	global_atomic_add v187, v224, s[6:7] offset:1536
	global_atomic_add v187, v224, s[6:7] offset:1792
	global_atomic_add v187, v224, s[6:7] offset:2048
	global_atomic_add v187, v224, s[6:7] offset:2304
	global_atomic_add v187, v224, s[6:7] offset:2560
	global_atomic_add v187, v224, s[6:7] offset:2816
	global_atomic_add v187, v224, s[6:7] offset:3072
	global_atomic_add v187, v224, s[6:7] offset:3328
	global_atomic_add v187, v224, s[6:7] offset:3584
	global_atomic_add v187, v224, s[6:7] offset:3840
.LBB0_251:
	s_or_b64 exec, exec, s[4:5]
	v_readlane_b32 s4, v251, 32
	v_readlane_b32 s5, v251, 33
	s_waitcnt vmcnt(0)
.LBB0_252:
	s_or_b64 exec, exec, s[0:1]
	s_waitcnt lgkmcnt(0)
	s_barrier

; __device__ __forceinline__ unsigned xb_ld(unsigned* p)              { return __hip_atomic_load(p, __ATOMIC_RELAXED, __HIP_MEMORY_SCOPE_AGENT); }
; __device__ __forceinline__ unsigned xb_add(unsigned* p, unsigned v) { return __hip_atomic_fetch_add(p, v, __ATOMIC_RELAXED, __HIP_MEMORY_SCOPE_AGENT); }
; #define XB_SPIN(cond, bar) do { unsigned _sp = 0; while (cond) { __builtin_amdgcn_s_sleep(1); \
;     if ((++_sp & 255u) == 0u) { if (xb_ld(&(bar)[XB_TMO])) break; if (_sp > XB_SPIN_CAP) { atomicAdd(&(bar)[XB_TMO], 1u); break; } } } } while (0)
; __device__ __forceinline__ void xcd_barrier(const XcdBarrier& b) {
;     ...
;         if (old + 1u == (gen + 1u) * nloc) {
;             __builtin_amdgcn_fence(__ATOMIC_RELEASE, "agent");
;             asm volatile("s_waitcnt vmcnt(0)" ::: "memory");
;             const unsigned og = xb_add(&bar[XB_TOP], 1u);
;             const unsigned tg = og / nx;
;             if (og + 1u == (tg + 1u) * nx) xb_add(&bar[XB_TOPGEN], 1u);
;             else XB_SPIN(xb_ld(&bar[XB_TOPGEN]) == tg, bar);
.LBB0_375:
	s_or_b64 exec, exec, s[6:7]
	s_waitcnt vmcnt(0)
	v_readfirstlane_b32 s4, v3
	v_sub_u32_e32 v4, 0, v2
	s_mov_b64 s[6:7], -1
	v_add_u32_e32 v3, s4, v1
	v_cvt_f32_u32_e32 v1, v2
	v_readlane_b32 s4, v251, 36
	v_readlane_b32 s5, v251, 37
	v_rcp_iflag_f32_e32 v1, v1
	s_nop 0
	v_mul_f32_e32 v1, 0x4f7ffffe, v1
	v_cvt_u32_f32_e32 v1, v1
	v_mul_lo_u32 v4, v4, v1
	v_mul_hi_u32 v4, v1, v4
	v_add_u32_e32 v1, v1, v4
	v_mul_hi_u32 v1, v3, v1
	v_mul_lo_u32 v4, v1, v2
	v_sub_u32_e32 v4, v3, v4
	v_cmp_ge_u32_e32 vcc, v4, v2
	v_add_u32_e32 v5, 1, v1
	v_add_u32_e32 v3, 1, v3
	v_cndmask_b32_e32 v1, v1, v5, vcc
	v_sub_u32_e32 v5, v4, v2
	v_cndmask_b32_e32 v4, v4, v5, vcc
	v_cmp_ge_u32_e32 vcc, v4, v2
	v_add_u32_e32 v4, 1, v1
	s_nop 0
	v_cndmask_b32_e32 v1, v1, v4, vcc
	v_mul_lo_u32 v4, v2, v1
	v_add_u32_e32 v2, v4, v2
	v_cmp_ne_u32_e32 vcc, v3, v2
	v_mov_b64_e32 v[2:3], s[4:5]
	s_and_saveexec_b64 s[4:5], vcc
	s_cbranch_execz .LBB0_387
	v_readlane_b32 s6, v251, 32
	v_readlane_b32 s7, v251, 33
	s_mov_b64 s[8:9], 0
	s_nop 3
	global_load_dword v2, v187, s[6:7] sc1
	s_waitcnt vmcnt(0)
	v_cmp_eq_u32_e32 vcc, v2, v1
	s_and_saveexec_b64 s[6:7], vcc
	s_cbranch_execz .LBB0_386
	s_mov_b32 s20, 1
	s_branch .LBB0_379

; __device__ __forceinline__ unsigned xb_ld(unsigned* p)              { return __hip_atomic_load(p, __ATOMIC_RELAXED, __HIP_MEMORY_SCOPE_AGENT); }
; __device__ __forceinline__ unsigned xb_add(unsigned* p, unsigned v) { return __hip_atomic_fetch_add(p, v, __ATOMIC_RELAXED, __HIP_MEMORY_SCOPE_AGENT); }
; #define XB_SPIN(cond, bar) do { unsigned _sp = 0; while (cond) { __builtin_amdgcn_s_sleep(1); \
;     if ((++_sp & 255u) == 0u) { if (xb_ld(&(bar)[XB_TMO])) break; if (_sp > XB_SPIN_CAP) { atomicAdd(&(bar)[XB_TMO], 1u); break; } } } } while (0)
; __device__ __forceinline__ void xcd_barrier(const XcdBarrier& b) {
;     ...
;             const unsigned og = xb_add(&bar[XB_TOP], 1u);
;             const unsigned tg = og / nx;
;             if (og + 1u == (tg + 1u) * nx) xb_add(&bar[XB_TOPGEN], 1u);
;             else XB_SPIN(xb_ld(&bar[XB_TOPGEN]) == tg, bar);
;             __builtin_amdgcn_fence(__ATOMIC_ACQUIRE, "agent");
;             xb_add(&bar[XB_XGEN(b.x)], 1u);
;             asm volatile("s_waitcnt vmcnt(0)" ::: "memory");
.LBB0_389:
	s_or_b64 exec, exec, s[4:5]
	v_readlane_b32 s4, v251, 32
	v_readlane_b32 s5, v251, 33
	s_waitcnt vmcnt(0)
.LBB0_390:
	s_or_b64 exec, exec, s[0:1]
	v_readlane_b32 s6, v250, 2
	v_readlane_b32 s7, v250, 3
	s_waitcnt lgkmcnt(0)
	s_barrier

; __device__ __forceinline__ unsigned xb_ld(unsigned* p)              { return __hip_atomic_load(p, __ATOMIC_RELAXED, __HIP_MEMORY_SCOPE_AGENT); }
; __device__ __forceinline__ unsigned xb_add(unsigned* p, unsigned v) { return __hip_atomic_fetch_add(p, v, __ATOMIC_RELAXED, __HIP_MEMORY_SCOPE_AGENT); }
; #define XB_SPIN(cond, bar) do { unsigned _sp = 0; while (cond) { __builtin_amdgcn_s_sleep(1); \
;     if ((++_sp & 255u) == 0u) { if (xb_ld(&(bar)[XB_TMO])) break; if (_sp > XB_SPIN_CAP) { atomicAdd(&(bar)[XB_TMO], 1u); break; } } } } while (0)
; __device__ __forceinline__ void xcd_barrier(const XcdBarrier& b) {
;     ...
;             const unsigned og = xb_add(&bar[XB_TOP], 1u);
;             const unsigned tg = og / nx;
;             if (og + 1u == (tg + 1u) * nx) xb_add(&bar[XB_TOPGEN], 1u);
;             else XB_SPIN(xb_ld(&bar[XB_TOPGEN]) == tg, bar);
;             __builtin_amdgcn_fence(__ATOMIC_ACQUIRE, "agent");
;             xb_add(&bar[XB_XGEN(b.x)], 1u);
;             asm volatile("s_waitcnt vmcnt(0)" ::: "memory");
.LBB0_580:
	s_or_b64 exec, exec, s[4:5]
	v_readlane_b32 s4, v251, 32
	v_readlane_b32 s5, v251, 33
	s_waitcnt vmcnt(0)
.LBB0_581:
	s_or_b64 exec, exec, s[0:1]
	s_waitcnt lgkmcnt(0)
	s_barrier

; __device__ __forceinline__ unsigned xb_ld(unsigned* p)              { return __hip_atomic_load(p, __ATOMIC_RELAXED, __HIP_MEMORY_SCOPE_AGENT); }
; __device__ __forceinline__ unsigned xb_add(unsigned* p, unsigned v) { return __hip_atomic_fetch_add(p, v, __ATOMIC_RELAXED, __HIP_MEMORY_SCOPE_AGENT); }
; #define XB_SPIN(cond, bar) do { unsigned _sp = 0; while (cond) { __builtin_amdgcn_s_sleep(1); \
;     if ((++_sp & 255u) == 0u) { if (xb_ld(&(bar)[XB_TMO])) break; if (_sp > XB_SPIN_CAP) { atomicAdd(&(bar)[XB_TMO], 1u); break; } } } } while (0)
; __device__ __forceinline__ void xcd_barrier(const XcdBarrier& b) {
;     ...
;             const unsigned og = xb_add(&bar[XB_TOP], 1u);
;             const unsigned tg = og / nx;
;             if (og + 1u == (tg + 1u) * nx) xb_add(&bar[XB_TOPGEN], 1u);
;             else XB_SPIN(xb_ld(&bar[XB_TOPGEN]) == tg, bar);
;             __builtin_amdgcn_fence(__ATOMIC_ACQUIRE, "agent");
;             xb_add(&bar[XB_XGEN(b.x)], 1u);
;             asm volatile("s_waitcnt vmcnt(0)" ::: "memory");
.LBB0_673:
	s_or_b64 exec, exec, s[4:5]
	v_readlane_b32 s4, v251, 32
	v_readlane_b32 s5, v251, 33
	s_waitcnt vmcnt(0)
.LBB0_674:
	s_or_b64 exec, exec, s[0:1]
	s_waitcnt lgkmcnt(0)
	s_barrier

; __device__ __forceinline__ unsigned xb_ld(unsigned* p)              { return __hip_atomic_load(p, __ATOMIC_RELAXED, __HIP_MEMORY_SCOPE_AGENT); }
; __device__ __forceinline__ unsigned xb_add(unsigned* p, unsigned v) { return __hip_atomic_fetch_add(p, v, __ATOMIC_RELAXED, __HIP_MEMORY_SCOPE_AGENT); }
; #define XB_SPIN(cond, bar) do { unsigned _sp = 0; while (cond) { __builtin_amdgcn_s_sleep(1); \
;     if ((++_sp & 255u) == 0u) { if (xb_ld(&(bar)[XB_TMO])) break; if (_sp > XB_SPIN_CAP) { atomicAdd(&(bar)[XB_TMO], 1u); break; } } } } while (0)
; __device__ __forceinline__ void xcd_barrier(const XcdBarrier& b) {
;     ...
;             const unsigned og = xb_add(&bar[XB_TOP], 1u);
;             const unsigned tg = og / nx;
;             if (og + 1u == (tg + 1u) * nx) xb_add(&bar[XB_TOPGEN], 1u);
;             else XB_SPIN(xb_ld(&bar[XB_TOPGEN]) == tg, bar);
;             __builtin_amdgcn_fence(__ATOMIC_ACQUIRE, "agent");
;             xb_add(&bar[XB_XGEN(b.x)], 1u);
;             asm volatile("s_waitcnt vmcnt(0)" ::: "memory");
.LBB0_746:
	s_or_b64 exec, exec, s[4:5]
	v_readlane_b32 s4, v251, 32
	v_readlane_b32 s5, v251, 33
	s_waitcnt vmcnt(0)
.LBB0_747:
	s_or_b64 exec, exec, s[0:1]
	s_waitcnt lgkmcnt(0)
	s_barrier

; __device__ __forceinline__ unsigned xb_ld(unsigned* p)              { return __hip_atomic_load(p, __ATOMIC_RELAXED, __HIP_MEMORY_SCOPE_AGENT); }
; __device__ __forceinline__ unsigned xb_add(unsigned* p, unsigned v) { return __hip_atomic_fetch_add(p, v, __ATOMIC_RELAXED, __HIP_MEMORY_SCOPE_AGENT); }
; #define XB_SPIN(cond, bar) do { unsigned _sp = 0; while (cond) { __builtin_amdgcn_s_sleep(1); \
;     if ((++_sp & 255u) == 0u) { if (xb_ld(&(bar)[XB_TMO])) break; if (_sp > XB_SPIN_CAP) { atomicAdd(&(bar)[XB_TMO], 1u); break; } } } } while (0)
; __device__ __forceinline__ void xcd_barrier(const XcdBarrier& b) {
;     ...
;         if (old + 1u == (gen + 1u) * nloc) {
;             __builtin_amdgcn_fence(__ATOMIC_RELEASE, "agent");
;             asm volatile("s_waitcnt vmcnt(0)" ::: "memory");
;             const unsigned og = xb_add(&bar[XB_TOP], 1u);
;             const unsigned tg = og / nx;
;             if (og + 1u == (tg + 1u) * nx) xb_add(&bar[XB_TOPGEN], 1u);
;             else XB_SPIN(xb_ld(&bar[XB_TOPGEN]) == tg, bar);
.LBB0_815:
	s_or_b64 exec, exec, s[8:9]
	s_waitcnt vmcnt(0)
	v_readfirstlane_b32 s6, v3
	v_sub_u32_e32 v4, 0, v2
	s_mov_b64 s[8:9], -1
	v_add_u32_e32 v3, s6, v1
	v_cvt_f32_u32_e32 v1, v2
	v_readlane_b32 s6, v251, 36
	v_readlane_b32 s7, v251, 37
	v_rcp_iflag_f32_e32 v1, v1
	s_nop 0
	v_mul_f32_e32 v1, 0x4f7ffffe, v1
	v_cvt_u32_f32_e32 v1, v1
	v_mul_lo_u32 v4, v4, v1
	v_mul_hi_u32 v4, v1, v4
	v_add_u32_e32 v1, v1, v4
	v_mul_hi_u32 v1, v3, v1
	v_mul_lo_u32 v4, v1, v2
	v_sub_u32_e32 v4, v3, v4
	v_cmp_ge_u32_e32 vcc, v4, v2
	v_add_u32_e32 v5, 1, v1
	v_add_u32_e32 v3, 1, v3
	v_cndmask_b32_e32 v1, v1, v5, vcc
	v_sub_u32_e32 v5, v4, v2
	v_cndmask_b32_e32 v4, v4, v5, vcc
	v_cmp_ge_u32_e32 vcc, v4, v2
	v_add_u32_e32 v4, 1, v1
	s_nop 0
	v_cndmask_b32_e32 v1, v1, v4, vcc
	v_mul_lo_u32 v4, v2, v1
	v_add_u32_e32 v2, v4, v2
	v_cmp_ne_u32_e32 vcc, v3, v2
	v_mov_b64_e32 v[2:3], s[6:7]
	s_and_saveexec_b64 s[6:7], vcc
	s_cbranch_execz .LBB0_827
	v_readlane_b32 s8, v251, 32
	v_readlane_b32 s9, v251, 33
	s_mov_b64 s[10:11], 0
	s_nop 3
	global_load_dword v2, v187, s[8:9] sc1
	s_waitcnt vmcnt(0)
	v_cmp_eq_u32_e32 vcc, v2, v1
	s_and_saveexec_b64 s[8:9], vcc
	s_cbranch_execz .LBB0_826
	s_mov_b32 s23, 1
	s_branch .LBB0_819

; __device__ __forceinline__ unsigned xb_ld(unsigned* p)              { return __hip_atomic_load(p, __ATOMIC_RELAXED, __HIP_MEMORY_SCOPE_AGENT); }
; __device__ __forceinline__ unsigned xb_add(unsigned* p, unsigned v) { return __hip_atomic_fetch_add(p, v, __ATOMIC_RELAXED, __HIP_MEMORY_SCOPE_AGENT); }
; #define XB_SPIN(cond, bar) do { unsigned _sp = 0; while (cond) { __builtin_amdgcn_s_sleep(1); \
;     if ((++_sp & 255u) == 0u) { if (xb_ld(&(bar)[XB_TMO])) break; if (_sp > XB_SPIN_CAP) { atomicAdd(&(bar)[XB_TMO], 1u); break; } } } } while (0)
; __device__ __forceinline__ void xcd_barrier(const XcdBarrier& b) {
;     ...
;             const unsigned og = xb_add(&bar[XB_TOP], 1u);
;             const unsigned tg = og / nx;
;             if (og + 1u == (tg + 1u) * nx) xb_add(&bar[XB_TOPGEN], 1u);
;             else XB_SPIN(xb_ld(&bar[XB_TOPGEN]) == tg, bar);
;             __builtin_amdgcn_fence(__ATOMIC_ACQUIRE, "agent");
;             xb_add(&bar[XB_XGEN(b.x)], 1u);
;             asm volatile("s_waitcnt vmcnt(0)" ::: "memory");
.LBB0_827:
	s_or_b64 exec, exec, s[6:7]
	s_and_saveexec_b64 s[6:7], s[8:9]
	s_cbranch_execz .LBB0_829
	global_atomic_add v[2:3], v224, off
	v_readlane_b32 s8, v250, 28
	v_readlane_b32 s9, v250, 29
	s_nop 0
	s_add_u32 s8, s8, 0x2200
	s_addc_u32 s9, s9, 0
	s_nop 0
	global_atomic_add v187, v224, s[8:9]
	global_atomic_add v187, v224, s[8:9] offset:256
	global_atomic_add v187, v224, s[8:9] offset:512
	global_atomic_add v187, v224, s[8:9] offset:768
	global_atomic_add v187, v224, s[8:9] offset:1024
	global_atomic_add v187, v224, s[8:9] offset:1280
	global_atomic_add v187, v224, s[8:9] offset:1536
	global_atomic_add v187, v224, s[8:9] offset:1792
	global_atomic_add v187, v224, s[8:9] offset:2048
	global_atomic_add v187, v224, s[8:9] offset:2304
	global_atomic_add v187, v224, s[8:9] offset:2560
	global_atomic_add v187, v224, s[8:9] offset:2816
	global_atomic_add v187, v224, s[8:9] offset:3072
	global_atomic_add v187, v224, s[8:9] offset:3328
	global_atomic_add v187, v224, s[8:9] offset:3584
	global_atomic_add v187, v224, s[8:9] offset:3840
.LBB0_829:
	s_or_b64 exec, exec, s[6:7]
	v_readlane_b32 s6, v251, 32
	v_readlane_b32 s7, v251, 33
	s_waitcnt vmcnt(0)
.LBB0_830:
	s_or_b64 exec, exec, s[4:5]
	s_waitcnt lgkmcnt(0)
	s_barrier

; __device__ __forceinline__ unsigned xb_ld(unsigned* p)              { return __hip_atomic_load(p, __ATOMIC_RELAXED, __HIP_MEMORY_SCOPE_AGENT); }
; __device__ __forceinline__ unsigned xb_add(unsigned* p, unsigned v) { return __hip_atomic_fetch_add(p, v, __ATOMIC_RELAXED, __HIP_MEMORY_SCOPE_AGENT); }
; #define XB_SPIN(cond, bar) do { unsigned _sp = 0; while (cond) { __builtin_amdgcn_s_sleep(1); \
;     if ((++_sp & 255u) == 0u) { if (xb_ld(&(bar)[XB_TMO])) break; if (_sp > XB_SPIN_CAP) { atomicAdd(&(bar)[XB_TMO], 1u); break; } } } } while (0)
; __device__ __forceinline__ void xcd_barrier(const XcdBarrier& b) {
;     ...
;             const unsigned og = xb_add(&bar[XB_TOP], 1u);
;             const unsigned tg = og / nx;
;             if (og + 1u == (tg + 1u) * nx) xb_add(&bar[XB_TOPGEN], 1u);
;             else XB_SPIN(xb_ld(&bar[XB_TOPGEN]) == tg, bar);
;             __builtin_amdgcn_fence(__ATOMIC_ACQUIRE, "agent");
;             xb_add(&bar[XB_XGEN(b.x)], 1u);
;             asm volatile("s_waitcnt vmcnt(0)" ::: "memory");
.LBB0_1049:
	s_or_b64 exec, exec, s[6:7]
	v_readlane_b32 s6, v251, 32
	v_readlane_b32 s7, v251, 33
	s_waitcnt vmcnt(0)
.LBB0_1050:
	s_or_b64 exec, exec, s[4:5]
	s_waitcnt lgkmcnt(0)
	s_barrier

; __device__ __forceinline__ unsigned xb_ld(unsigned* p)              { return __hip_atomic_load(p, __ATOMIC_RELAXED, __HIP_MEMORY_SCOPE_AGENT); }
; __device__ __forceinline__ unsigned xb_add(unsigned* p, unsigned v) { return __hip_atomic_fetch_add(p, v, __ATOMIC_RELAXED, __HIP_MEMORY_SCOPE_AGENT); }
; #define XB_SPIN(cond, bar) do { unsigned _sp = 0; while (cond) { __builtin_amdgcn_s_sleep(1); \
;     if ((++_sp & 255u) == 0u) { if (xb_ld(&(bar)[XB_TMO])) break; if (_sp > XB_SPIN_CAP) { atomicAdd(&(bar)[XB_TMO], 1u); break; } } } } while (0)
; __device__ __forceinline__ void xcd_barrier(const XcdBarrier& b) {
;     ...
;             const unsigned og = xb_add(&bar[XB_TOP], 1u);
;             const unsigned tg = og / nx;
;             if (og + 1u == (tg + 1u) * nx) xb_add(&bar[XB_TOPGEN], 1u);
;             else XB_SPIN(xb_ld(&bar[XB_TOPGEN]) == tg, bar);
;             __builtin_amdgcn_fence(__ATOMIC_ACQUIRE, "agent");
;             xb_add(&bar[XB_XGEN(b.x)], 1u);
;             asm volatile("s_waitcnt vmcnt(0)" ::: "memory");
.LBB0_1243:
	s_or_b64 exec, exec, s[4:5]
	v_readlane_b32 s4, v251, 32
	v_readlane_b32 s5, v251, 33
	s_waitcnt vmcnt(0)
.LBB0_1244:
	s_or_b64 exec, exec, s[0:1]
	s_waitcnt lgkmcnt(0)
	s_barrier

; __device__ __forceinline__ unsigned xb_ld(unsigned* p)              { return __hip_atomic_load(p, __ATOMIC_RELAXED, __HIP_MEMORY_SCOPE_AGENT); }
; __device__ __forceinline__ unsigned xb_add(unsigned* p, unsigned v) { return __hip_atomic_fetch_add(p, v, __ATOMIC_RELAXED, __HIP_MEMORY_SCOPE_AGENT); }
; #define XB_SPIN(cond, bar) do { unsigned _sp = 0; while (cond) { __builtin_amdgcn_s_sleep(1); \
;     if ((++_sp & 255u) == 0u) { if (xb_ld(&(bar)[XB_TMO])) break; if (_sp > XB_SPIN_CAP) { atomicAdd(&(bar)[XB_TMO], 1u); break; } } } } while (0)
; __device__ __forceinline__ void xcd_barrier(const XcdBarrier& b) {
;     ...
;             const unsigned og = xb_add(&bar[XB_TOP], 1u);
;             const unsigned tg = og / nx;
;             if (og + 1u == (tg + 1u) * nx) xb_add(&bar[XB_TOPGEN], 1u);
;             else XB_SPIN(xb_ld(&bar[XB_TOPGEN]) == tg, bar);
;             __builtin_amdgcn_fence(__ATOMIC_ACQUIRE, "agent");
;             xb_add(&bar[XB_XGEN(b.x)], 1u);
;             asm volatile("s_waitcnt vmcnt(0)" ::: "memory");
.LBB0_1343:
	s_or_b64 exec, exec, s[4:5]
	v_readlane_b32 s4, v251, 32
	v_readlane_b32 s5, v251, 33
	s_waitcnt vmcnt(0)
.LBB0_1344:
	s_or_b64 exec, exec, s[0:1]
	s_waitcnt lgkmcnt(0)
	s_barrier
